# spatial: five key blocks of the max pass stay in registers, only two QK blocks recomputed
# speedup vs baseline: 1.0358x; 1.0003x over previous
_Z9k_spatialPKDF16_S0_S0_PfPDF16_:
	s_load_dwordx4 s[4:7], s[0:1], 0x0
	s_load_dwordx2 s[10:11], s[0:1], 0x10
	s_mul_hi_i32 s9, s2, 0x3140
	s_mul_i32 s8, s2, 0x3140
	s_lshl_b64 s[8:9], s[8:9], 1
	v_and_b32_e32 v2, 7, v0
	v_lshrrev_b32_e32 v3, 3, v0
	v_lshlrev_b32_e32 v10, 4, v2
	v_lshl_or_b32 v4, v3, 7, v10
	v_add_u32_e32 v5, 0x1c00, v4
	v_add_u32_e32 v6, 0x3800, v4
	v_add_u32_e32 v7, 0x5400, v4
	v_lshrrev_b32_e32 v8, 1, v0
	v_and_b32_e32 v108, 31, v0
	v_and_b32_e32 v115, 0xe0, v8
	v_or_b32_e32 v109, v115, v108
	s_movk_i32 s3, 0xc5
	v_mov_b32_e32 v8, 0xc4
	v_cmp_gt_u32_e64 s[12:13], s3, v109
	v_bfe_u32 v1, v0, 5, 1
	v_lshlrev_b32_e32 v111, 4, v1
	s_nop 1
	v_cndmask_b32_e64 v110, v8, v109, s[12:13]
	v_lshl_or_b32 v9, v110, 7, v111
	s_movk_i32 s3, 0xe8
	v_cmp_gt_u32_e32 vcc, s3, v0
	v_or_b32_e32 v14, 0x6200, v10
	s_nop 1
	v_cndmask_b32_e32 v7, v14, v7, vcc
	s_waitcnt lgkmcnt(0)
	s_add_u32 s6, s6, s8
	s_addc_u32 s7, s7, s9
	s_add_u32 s10, s10, s8
	s_addc_u32 s11, s11, s9
	s_add_u32 s4, s4, s8
	s_addc_u32 s5, s5, s9
	global_load_dwordx4 v[18:21], v4, s[6:7] nt
	global_load_dwordx4 v[22:25], v4, s[10:11] nt
	global_load_dwordx4 v[26:29], v5, s[6:7] nt
	global_load_dwordx4 v[30:33], v5, s[10:11] nt
	global_load_dwordx4 v[34:37], v6, s[6:7] nt
	global_load_dwordx4 v[38:41], v6, s[10:11] nt
	global_load_dwordx4 v[42:45], v7, s[6:7] nt
	global_load_dwordx4 v[46:49], v7, s[10:11] nt
	global_load_dwordx4 v[74:77], v9, s[4:5] offset:0 nt
	global_load_dwordx4 v[78:81], v9, s[4:5] offset:32 nt
	global_load_dwordx4 v[82:85], v9, s[4:5] offset:64 nt
	global_load_dwordx4 v[86:89], v9, s[4:5] offset:96 nt
	s_movk_i32 s3, 0x90
	v_lshlrev_b32_e32 v11, 3, v2
	v_mul_u32_u24_e32 v16, 0x1c8, v11
	v_mad_u32_u24 v12, v3, s3, v10
	v_lshl_add_u32 v13, v3, 1, v16
	v_mad_u32_u24 v112, v108, s3, v111
	s_waitcnt vmcnt(11)
	ds_write_b128 v12, v[18:21] offset:0
	s_waitcnt vmcnt(10)
	ds_write_b16 v13, v22 offset:32256
	ds_write_b16_d16_hi v13, v22 offset:32712
	ds_write_b16 v13, v23 offset:33168
	ds_write_b16_d16_hi v13, v23 offset:33624
	ds_write_b16 v13, v24 offset:34080
	ds_write_b16_d16_hi v13, v24 offset:34536
	ds_write_b16 v13, v25 offset:34992
	ds_write_b16_d16_hi v13, v25 offset:35448
	s_waitcnt vmcnt(9)
	ds_write_b128 v12, v[26:29] offset:8064
	s_waitcnt vmcnt(8)
	ds_write_b16 v13, v30 offset:32368
	ds_write_b16_d16_hi v13, v30 offset:32824
	ds_write_b16 v13, v31 offset:33280
	ds_write_b16_d16_hi v13, v31 offset:33736
	ds_write_b16 v13, v32 offset:34192
	ds_write_b16_d16_hi v13, v32 offset:34648
	ds_write_b16 v13, v33 offset:35104
	ds_write_b16_d16_hi v13, v33 offset:35560
	s_waitcnt vmcnt(7)
	ds_write_b128 v12, v[34:37] offset:16128
	s_waitcnt vmcnt(6)
	ds_write_b16 v13, v38 offset:32480
	ds_write_b16_d16_hi v13, v38 offset:32936
	ds_write_b16 v13, v39 offset:33392
	ds_write_b16_d16_hi v13, v39 offset:33848
	ds_write_b16 v13, v40 offset:34304
	ds_write_b16_d16_hi v13, v40 offset:34760
	ds_write_b16 v13, v41 offset:35216
	ds_write_b16_d16_hi v13, v41 offset:35672
	s_waitcnt vmcnt(5)
	v_cndmask_b32_e32 v42, 0, v42, vcc
	v_cndmask_b32_e32 v43, 0, v43, vcc
	v_cndmask_b32_e32 v44, 0, v44, vcc
	v_cndmask_b32_e32 v45, 0, v45, vcc
	ds_write_b128 v12, v[42:45] offset:24192
	s_waitcnt vmcnt(4)
	v_cndmask_b32_e32 v46, 0, v46, vcc
	v_cndmask_b32_e32 v47, 0, v47, vcc
	v_cndmask_b32_e32 v48, 0, v48, vcc
	v_cndmask_b32_e32 v49, 0, v49, vcc
	ds_write_b16 v13, v46 offset:32592
	ds_write_b16_d16_hi v13, v46 offset:33048
	ds_write_b16 v13, v47 offset:33504
	ds_write_b16_d16_hi v13, v47 offset:33960
	ds_write_b16 v13, v48 offset:34416
	ds_write_b16_d16_hi v13, v48 offset:34872
	ds_write_b16 v13, v49 offset:35328
	ds_write_b16_d16_hi v13, v49 offset:35784
	s_load_dwordx2 s[8:9], s[0:1], 0x20
	s_load_dwordx2 s[10:11], s[0:1], 0x18
	s_mov_b32 s16, 0x3e38aa3b
	s_mov_b32 s17, 0xf149f2ca
	v_cmp_eq_u32_e64 s[14:15], 0, v1
	v_mul_u32_u24_e32 v113, 0x1c8, v108
	v_lshl_add_u32 v113, v1, 3, v113
	v_add_u32_e32 v113, 0x7e00, v113
	v_add_u32_e32 v114, 0x3900, v113
	v_mov_b32_e32 v106, s17
	s_waitcnt vmcnt(0) lgkmcnt(0)
	s_barrier
	ds_read_b128 v[66:69], v112 offset:0
	ds_read_b128 v[70:73], v112 offset:32
	s_waitcnt lgkmcnt(1)
	v_mfma_f32_32x32x16_f16 v[2:17], v[66:69], v[74:77], 0
	ds_read_b128 v[66:69], v112 offset:64
	s_waitcnt lgkmcnt(1)
	v_mfma_f32_32x32x16_f16 v[2:17], v[70:73], v[78:81], v[2:17]
	ds_read_b128 v[70:73], v112 offset:96
	s_waitcnt lgkmcnt(1)
	v_mfma_f32_32x32x16_f16 v[2:17], v[66:69], v[82:85], v[2:17]
	s_waitcnt lgkmcnt(0)
	v_mfma_f32_32x32x16_f16 v[2:17], v[70:73], v[86:89], v[2:17]
	ds_read_b128 v[66:69], v112 offset:4608
	ds_read_b128 v[70:73], v112 offset:4640
	s_waitcnt lgkmcnt(1)
	v_mfma_f32_32x32x16_f16 v[50:65], v[66:69], v[74:77], 0
	ds_read_b128 v[66:69], v112 offset:4672
	s_waitcnt lgkmcnt(1)
	v_mfma_f32_32x32x16_f16 v[50:65], v[70:73], v[78:81], v[50:65]
	ds_read_b128 v[70:73], v112 offset:4704
	s_waitcnt lgkmcnt(1)
	v_mfma_f32_32x32x16_f16 v[50:65], v[66:69], v[82:85], v[50:65]
	s_waitcnt lgkmcnt(0)
	v_mfma_f32_32x32x16_f16 v[50:65], v[70:73], v[86:89], v[50:65]
	v_max3_f32 v106, v106, v2, v3
	v_max3_f32 v106, v106, v4, v5
	v_max3_f32 v106, v106, v6, v7
	v_max3_f32 v106, v106, v8, v9
	v_max3_f32 v106, v106, v10, v11
	v_max3_f32 v106, v106, v12, v13
	v_max3_f32 v106, v106, v14, v15
	v_max3_f32 v106, v106, v16, v17
	ds_read_b128 v[66:69], v112 offset:9216
	ds_read_b128 v[70:73], v112 offset:9248
	s_waitcnt lgkmcnt(1)
	v_mfma_f32_32x32x16_f16 v[2:17], v[66:69], v[74:77], 0
	ds_read_b128 v[66:69], v112 offset:9280
	s_waitcnt lgkmcnt(1)
	v_mfma_f32_32x32x16_f16 v[2:17], v[70:73], v[78:81], v[2:17]
	ds_read_b128 v[70:73], v112 offset:9312
	s_waitcnt lgkmcnt(1)
	v_mfma_f32_32x32x16_f16 v[2:17], v[66:69], v[82:85], v[2:17]
	s_waitcnt lgkmcnt(0)
	v_mfma_f32_32x32x16_f16 v[2:17], v[70:73], v[86:89], v[2:17]
	v_max3_f32 v106, v106, v50, v51
	v_max3_f32 v106, v106, v52, v53
	v_max3_f32 v106, v106, v54, v55
	v_max3_f32 v106, v106, v56, v57
	v_max3_f32 v106, v106, v58, v59
	v_max3_f32 v106, v106, v60, v61
	v_max3_f32 v106, v106, v62, v63
	v_max3_f32 v106, v106, v64, v65
	ds_read_b128 v[66:69], v112 offset:13824
	ds_read_b128 v[70:73], v112 offset:13856
	s_waitcnt lgkmcnt(1)
	v_mfma_f32_32x32x16_f16 v[50:65], v[66:69], v[74:77], 0
	ds_read_b128 v[66:69], v112 offset:13888
	s_waitcnt lgkmcnt(1)
	v_mfma_f32_32x32x16_f16 v[50:65], v[70:73], v[78:81], v[50:65]
	ds_read_b128 v[70:73], v112 offset:13920
	s_waitcnt lgkmcnt(1)
	v_mfma_f32_32x32x16_f16 v[50:65], v[66:69], v[82:85], v[50:65]
	s_waitcnt lgkmcnt(0)
	v_mfma_f32_32x32x16_f16 v[50:65], v[70:73], v[86:89], v[50:65]
	v_max3_f32 v106, v106, v2, v3
	v_max3_f32 v106, v106, v4, v5
	v_max3_f32 v106, v106, v6, v7
	v_max3_f32 v106, v106, v8, v9
	v_max3_f32 v106, v106, v10, v11
	v_max3_f32 v106, v106, v12, v13
	v_max3_f32 v106, v106, v14, v15
	v_max3_f32 v106, v106, v16, v17
	ds_read_b128 v[66:69], v112 offset:18432
	ds_read_b128 v[70:73], v112 offset:18464
	s_waitcnt lgkmcnt(1)
	v_mfma_f32_32x32x16_f16 v[18:33], v[66:69], v[74:77], 0
	ds_read_b128 v[66:69], v112 offset:18496
	s_waitcnt lgkmcnt(1)
	v_mfma_f32_32x32x16_f16 v[18:33], v[70:73], v[78:81], v[18:33]
	ds_read_b128 v[70:73], v112 offset:18528
	s_waitcnt lgkmcnt(1)
	v_mfma_f32_32x32x16_f16 v[18:33], v[66:69], v[82:85], v[18:33]
	s_waitcnt lgkmcnt(0)
	v_mfma_f32_32x32x16_f16 v[18:33], v[70:73], v[86:89], v[18:33]
	v_max3_f32 v106, v106, v50, v51
	v_max3_f32 v106, v106, v52, v53
	v_max3_f32 v106, v106, v54, v55
	v_max3_f32 v106, v106, v56, v57
	v_max3_f32 v106, v106, v58, v59
	v_max3_f32 v106, v106, v60, v61
	v_max3_f32 v106, v106, v62, v63
	v_max3_f32 v106, v106, v64, v65
	ds_read_b128 v[66:69], v112 offset:23040
	ds_read_b128 v[70:73], v112 offset:23072
	s_waitcnt lgkmcnt(1)
	v_mfma_f32_32x32x16_f16 v[34:49], v[66:69], v[74:77], 0
	ds_read_b128 v[66:69], v112 offset:23104
	s_waitcnt lgkmcnt(1)
	v_mfma_f32_32x32x16_f16 v[34:49], v[70:73], v[78:81], v[34:49]
	ds_read_b128 v[70:73], v112 offset:23136
	s_waitcnt lgkmcnt(1)
	v_mfma_f32_32x32x16_f16 v[34:49], v[66:69], v[82:85], v[34:49]
	s_waitcnt lgkmcnt(0)
	v_mfma_f32_32x32x16_f16 v[34:49], v[70:73], v[86:89], v[34:49]
	v_max3_f32 v106, v106, v18, v19
	v_max3_f32 v106, v106, v20, v21
	v_max3_f32 v106, v106, v22, v23
	v_max3_f32 v106, v106, v24, v25
	v_max3_f32 v106, v106, v26, v27
	v_max3_f32 v106, v106, v28, v29
	v_max3_f32 v106, v106, v30, v31
	v_max3_f32 v106, v106, v32, v33
	ds_read_b128 v[66:69], v112 offset:27648
	ds_read_b128 v[70:73], v112 offset:27680
	s_waitcnt lgkmcnt(1)
	v_mfma_f32_32x32x16_f16 v[90:105], v[66:69], v[74:77], 0
	ds_read_b128 v[66:69], v112 offset:27712
	s_waitcnt lgkmcnt(1)
	v_mfma_f32_32x32x16_f16 v[90:105], v[70:73], v[78:81], v[90:105]
	ds_read_b128 v[70:73], v112 offset:27744
	s_waitcnt lgkmcnt(1)
	v_mfma_f32_32x32x16_f16 v[90:105], v[66:69], v[82:85], v[90:105]
	s_waitcnt lgkmcnt(0)
	v_mfma_f32_32x32x16_f16 v[90:105], v[70:73], v[86:89], v[90:105]
	v_max3_f32 v106, v106, v34, v35
	v_max3_f32 v106, v106, v36, v37
	v_max3_f32 v106, v106, v38, v39
	v_max3_f32 v106, v106, v40, v41
	v_max3_f32 v106, v106, v42, v43
	v_max3_f32 v106, v106, v44, v45
	v_max3_f32 v106, v106, v46, v47
	v_max3_f32 v106, v106, v48, v49
	s_nop 15
	s_nop 1
	v_mov_b32_e32 v94, s17
	v_mov_b32_e32 v95, s17
	v_mov_b32_e32 v96, s17
	v_mov_b32_e32 v97, s17
	v_mov_b32_e32 v98, s17
	v_mov_b32_e32 v99, s17
	v_mov_b32_e32 v100, s17
	v_mov_b32_e32 v101, s17
	v_mov_b32_e32 v102, s17
	v_mov_b32_e32 v103, s17
	v_mov_b32_e32 v104, s17
	v_mov_b32_e32 v105, s17
	v_mov_b32_e32 v120, s17
	v_cndmask_b32_e64 v91, v120, v91, s[14:15]
	v_cndmask_b32_e64 v92, v120, v92, s[14:15]
	v_cndmask_b32_e64 v93, v120, v93, s[14:15]
	v_max3_f32 v106, v106, v90, v91
	v_max3_f32 v106, v106, v92, v93
	v_max3_f32 v106, v106, v94, v95
	v_max3_f32 v106, v106, v96, v97
	v_max3_f32 v106, v106, v98, v99
	v_max3_f32 v106, v106, v100, v101
	v_max3_f32 v106, v106, v102, v103
	v_max3_f32 v106, v106, v104, v105
	v_mov_b32_e32 v120, v106
	v_mov_b32_e32 v121, v106
	s_nop 1
	v_permlane32_swap_b32_e32 v120, v121
	s_nop 1
	v_max3_f32 v106, v106, v120, v121
	v_mul_f32_e32 v106, s16, v106
	v_mov_b32_e32 v107, 0
	v_fma_f32 v120, v50, s16, -v106
	v_exp_f32_e32 v50, v120
	v_fma_f32 v121, v51, s16, -v106
	v_exp_f32_e32 v51, v121
	v_fma_f32 v122, v52, s16, -v106
	v_exp_f32_e32 v52, v122
	v_fma_f32 v123, v53, s16, -v106
	v_exp_f32_e32 v53, v123
	v_fma_f32 v120, v54, s16, -v106
	v_exp_f32_e32 v54, v120
	v_fma_f32 v121, v55, s16, -v106
	v_exp_f32_e32 v55, v121
	v_fma_f32 v122, v56, s16, -v106
	v_exp_f32_e32 v56, v122
	v_fma_f32 v123, v57, s16, -v106
	v_exp_f32_e32 v57, v123
	v_fma_f32 v120, v58, s16, -v106
	v_exp_f32_e32 v58, v120
	v_fma_f32 v121, v59, s16, -v106
	v_exp_f32_e32 v59, v121
	v_fma_f32 v122, v60, s16, -v106
	v_exp_f32_e32 v60, v122
	v_fma_f32 v123, v61, s16, -v106
	v_exp_f32_e32 v61, v123
	v_fma_f32 v120, v62, s16, -v106
	v_exp_f32_e32 v62, v120
	v_fma_f32 v121, v63, s16, -v106
	v_exp_f32_e32 v63, v121
	v_fma_f32 v122, v64, s16, -v106
	v_exp_f32_e32 v64, v122
	v_fma_f32 v123, v65, s16, -v106
	v_exp_f32_e32 v65, v123
	v_add_f32_e32 v107, v107, v50
	v_add_f32_e32 v107, v107, v51
	v_add_f32_e32 v107, v107, v52
	v_add_f32_e32 v107, v107, v53
	v_add_f32_e32 v107, v107, v54
	v_add_f32_e32 v107, v107, v55
	v_add_f32_e32 v107, v107, v56
	v_add_f32_e32 v107, v107, v57
	v_add_f32_e32 v107, v107, v58
	v_add_f32_e32 v107, v107, v59
	v_add_f32_e32 v107, v107, v60
	v_add_f32_e32 v107, v107, v61
	v_add_f32_e32 v107, v107, v62
	v_add_f32_e32 v107, v107, v63
	v_add_f32_e32 v107, v107, v64
	v_add_f32_e32 v107, v107, v65
	v_cvt_pk_f16_f32 v66, v50, v51
	v_cvt_pk_f16_f32 v67, v52, v53
	v_cvt_pk_f16_f32 v68, v54, v55
	v_cvt_pk_f16_f32 v69, v56, v57
	v_cvt_pk_f16_f32 v70, v58, v59
	v_cvt_pk_f16_f32 v71, v60, v61
	v_cvt_pk_f16_f32 v72, v62, v63
	v_cvt_pk_f16_f32 v73, v64, v65
	v_fma_f32 v120, v18, s16, -v106
	v_exp_f32_e32 v18, v120
	v_fma_f32 v121, v19, s16, -v106
	v_exp_f32_e32 v19, v121
	v_fma_f32 v122, v20, s16, -v106
	v_exp_f32_e32 v20, v122
	v_fma_f32 v123, v21, s16, -v106
	v_exp_f32_e32 v21, v123
	v_fma_f32 v120, v22, s16, -v106
	v_exp_f32_e32 v22, v120
	v_fma_f32 v121, v23, s16, -v106
	v_exp_f32_e32 v23, v121
	v_fma_f32 v122, v24, s16, -v106
	v_exp_f32_e32 v24, v122
	v_fma_f32 v123, v25, s16, -v106
	v_exp_f32_e32 v25, v123
	v_fma_f32 v120, v26, s16, -v106
	v_exp_f32_e32 v26, v120
	v_fma_f32 v121, v27, s16, -v106
	v_exp_f32_e32 v27, v121
	v_fma_f32 v122, v28, s16, -v106
	v_exp_f32_e32 v28, v122
	v_fma_f32 v123, v29, s16, -v106
	v_exp_f32_e32 v29, v123
	v_fma_f32 v120, v30, s16, -v106
	v_exp_f32_e32 v30, v120
	v_fma_f32 v121, v31, s16, -v106
	v_exp_f32_e32 v31, v121
	v_fma_f32 v122, v32, s16, -v106
	v_exp_f32_e32 v32, v122
	v_fma_f32 v123, v33, s16, -v106
	v_exp_f32_e32 v33, v123
	v_add_f32_e32 v107, v107, v18
	v_add_f32_e32 v107, v107, v19
	v_add_f32_e32 v107, v107, v20
	v_add_f32_e32 v107, v107, v21
	v_add_f32_e32 v107, v107, v22
	v_add_f32_e32 v107, v107, v23
	v_add_f32_e32 v107, v107, v24
	v_add_f32_e32 v107, v107, v25
	v_add_f32_e32 v107, v107, v26
	v_add_f32_e32 v107, v107, v27
	v_add_f32_e32 v107, v107, v28
	v_add_f32_e32 v107, v107, v29
	v_add_f32_e32 v107, v107, v30
	v_add_f32_e32 v107, v107, v31
	v_add_f32_e32 v107, v107, v32
	v_add_f32_e32 v107, v107, v33
	v_cvt_pk_f16_f32 v50, v18, v19
	v_cvt_pk_f16_f32 v51, v20, v21
	v_cvt_pk_f16_f32 v52, v22, v23
	v_cvt_pk_f16_f32 v53, v24, v25
	v_cvt_pk_f16_f32 v54, v26, v27
	v_cvt_pk_f16_f32 v55, v28, v29
	v_cvt_pk_f16_f32 v56, v30, v31
	v_cvt_pk_f16_f32 v57, v32, v33
	v_fma_f32 v120, v34, s16, -v106
	v_exp_f32_e32 v34, v120
	v_fma_f32 v121, v35, s16, -v106
	v_exp_f32_e32 v35, v121
	v_fma_f32 v122, v36, s16, -v106
	v_exp_f32_e32 v36, v122
	v_fma_f32 v123, v37, s16, -v106
	v_exp_f32_e32 v37, v123
	v_fma_f32 v120, v38, s16, -v106
	v_exp_f32_e32 v38, v120
	v_fma_f32 v121, v39, s16, -v106
	v_exp_f32_e32 v39, v121
	v_fma_f32 v122, v40, s16, -v106
	v_exp_f32_e32 v40, v122
	v_fma_f32 v123, v41, s16, -v106
	v_exp_f32_e32 v41, v123
	v_fma_f32 v120, v42, s16, -v106
	v_exp_f32_e32 v42, v120
	v_fma_f32 v121, v43, s16, -v106
	v_exp_f32_e32 v43, v121
	v_fma_f32 v122, v44, s16, -v106
	v_exp_f32_e32 v44, v122
	v_fma_f32 v123, v45, s16, -v106
	v_exp_f32_e32 v45, v123
	v_fma_f32 v120, v46, s16, -v106
	v_exp_f32_e32 v46, v120
	v_fma_f32 v121, v47, s16, -v106
	v_exp_f32_e32 v47, v121
	v_fma_f32 v122, v48, s16, -v106
	v_exp_f32_e32 v48, v122
	v_fma_f32 v123, v49, s16, -v106
	v_exp_f32_e32 v49, v123
	v_add_f32_e32 v107, v107, v34
	v_add_f32_e32 v107, v107, v35
	v_add_f32_e32 v107, v107, v36
	v_add_f32_e32 v107, v107, v37
	v_add_f32_e32 v107, v107, v38
	v_add_f32_e32 v107, v107, v39
	v_add_f32_e32 v107, v107, v40
	v_add_f32_e32 v107, v107, v41
	v_add_f32_e32 v107, v107, v42
	v_add_f32_e32 v107, v107, v43
	v_add_f32_e32 v107, v107, v44
	v_add_f32_e32 v107, v107, v45
	v_add_f32_e32 v107, v107, v46
	v_add_f32_e32 v107, v107, v47
	v_add_f32_e32 v107, v107, v48
	v_add_f32_e32 v107, v107, v49
	v_cvt_pk_f16_f32 v116, v34, v35
	v_cvt_pk_f16_f32 v117, v36, v37
	v_cvt_pk_f16_f32 v118, v38, v39
	v_cvt_pk_f16_f32 v119, v40, v41
	v_cvt_pk_f16_f32 v124, v42, v43
	v_cvt_pk_f16_f32 v125, v44, v45
	v_cvt_pk_f16_f32 v126, v46, v47
	v_cvt_pk_f16_f32 v127, v48, v49
	v_mov_b32_e32 v18, 0
	v_mov_b32_e32 v19, 0
	v_mov_b32_e32 v20, 0
	v_mov_b32_e32 v21, 0
	v_mov_b32_e32 v22, 0
	v_mov_b32_e32 v23, 0
	v_mov_b32_e32 v24, 0
	v_mov_b32_e32 v25, 0
	v_mov_b32_e32 v26, 0
	v_mov_b32_e32 v27, 0
	v_mov_b32_e32 v28, 0
	v_mov_b32_e32 v29, 0
	v_mov_b32_e32 v30, 0
	v_mov_b32_e32 v31, 0
	v_mov_b32_e32 v32, 0
	v_mov_b32_e32 v33, 0
	v_mov_b32_e32 v34, 0
	v_mov_b32_e32 v35, 0
	v_mov_b32_e32 v36, 0
	v_mov_b32_e32 v37, 0
	v_mov_b32_e32 v38, 0
	v_mov_b32_e32 v39, 0
	v_mov_b32_e32 v40, 0
	v_mov_b32_e32 v41, 0
	v_mov_b32_e32 v42, 0
	v_mov_b32_e32 v43, 0
	v_mov_b32_e32 v44, 0
	v_mov_b32_e32 v45, 0
	v_mov_b32_e32 v46, 0
	v_mov_b32_e32 v47, 0
	v_mov_b32_e32 v48, 0
	v_mov_b32_e32 v49, 0
	ds_read2_b64 v[58:61], v113 offset0:24 offset1:26
	ds_read2_b64 v[62:65], v114 offset0:24 offset1:26
	s_nop 1
	s_waitcnt lgkmcnt(1)
	v_mfma_f32_32x32x16_f16 v[18:33], v[58:61], v[66:69], v[18:33]
	ds_read2_b64 v[58:61], v113 offset0:28 offset1:30
	s_waitcnt lgkmcnt(1)
	v_mfma_f32_32x32x16_f16 v[34:49], v[62:65], v[66:69], v[34:49]
	ds_read2_b64 v[62:65], v114 offset0:28 offset1:30
	s_waitcnt lgkmcnt(1)
	v_mfma_f32_32x32x16_f16 v[18:33], v[58:61], v[70:73], v[18:33]
	s_waitcnt lgkmcnt(0)
	v_mfma_f32_32x32x16_f16 v[34:49], v[62:65], v[70:73], v[34:49]
	ds_read2_b64 v[58:61], v113 offset0:32 offset1:34
	ds_read2_b64 v[62:65], v114 offset0:32 offset1:34
	s_nop 1
	s_waitcnt lgkmcnt(1)
	v_mfma_f32_32x32x16_f16 v[18:33], v[58:61], v[50:53], v[18:33]
	ds_read2_b64 v[58:61], v113 offset0:36 offset1:38
	s_waitcnt lgkmcnt(1)
	v_mfma_f32_32x32x16_f16 v[34:49], v[62:65], v[50:53], v[34:49]
	ds_read2_b64 v[62:65], v114 offset0:36 offset1:38
	s_waitcnt lgkmcnt(1)
	v_mfma_f32_32x32x16_f16 v[18:33], v[58:61], v[54:57], v[18:33]
	s_waitcnt lgkmcnt(0)
	v_mfma_f32_32x32x16_f16 v[34:49], v[62:65], v[54:57], v[34:49]
	ds_read2_b64 v[58:61], v113 offset0:40 offset1:42
	ds_read2_b64 v[62:65], v114 offset0:40 offset1:42
	s_nop 1
	s_waitcnt lgkmcnt(1)
	v_mfma_f32_32x32x16_f16 v[18:33], v[58:61], v[116:119], v[18:33]
	ds_read2_b64 v[58:61], v113 offset0:44 offset1:46
	s_waitcnt lgkmcnt(1)
	v_mfma_f32_32x32x16_f16 v[34:49], v[62:65], v[116:119], v[34:49]
	ds_read2_b64 v[62:65], v114 offset0:44 offset1:46
	s_waitcnt lgkmcnt(1)
	v_mfma_f32_32x32x16_f16 v[18:33], v[58:61], v[124:127], v[18:33]
	s_waitcnt lgkmcnt(0)
	v_mfma_f32_32x32x16_f16 v[34:49], v[62:65], v[124:127], v[34:49]
	v_fma_f32 v120, v90, s16, -v106
	v_exp_f32_e32 v90, v120
	v_fma_f32 v121, v91, s16, -v106
	v_exp_f32_e32 v91, v121
	v_fma_f32 v122, v92, s16, -v106
	v_exp_f32_e32 v92, v122
	v_fma_f32 v123, v93, s16, -v106
	v_exp_f32_e32 v93, v123
	v_fma_f32 v120, v94, s16, -v106
	v_exp_f32_e32 v94, v120
	v_fma_f32 v121, v95, s16, -v106
	v_exp_f32_e32 v95, v121
	v_fma_f32 v122, v96, s16, -v106
	v_exp_f32_e32 v96, v122
	v_fma_f32 v123, v97, s16, -v106
	v_exp_f32_e32 v97, v123
	v_fma_f32 v120, v98, s16, -v106
	v_exp_f32_e32 v98, v120
	v_fma_f32 v121, v99, s16, -v106
	v_exp_f32_e32 v99, v121
	v_fma_f32 v122, v100, s16, -v106
	v_exp_f32_e32 v100, v122
	v_fma_f32 v123, v101, s16, -v106
	v_exp_f32_e32 v101, v123
	v_fma_f32 v120, v102, s16, -v106
	v_exp_f32_e32 v102, v120
	v_fma_f32 v121, v103, s16, -v106
	v_exp_f32_e32 v103, v121
	v_fma_f32 v122, v104, s16, -v106
	v_exp_f32_e32 v104, v122
	v_fma_f32 v123, v105, s16, -v106
	v_exp_f32_e32 v105, v123
	v_add_f32_e32 v107, v107, v90
	v_add_f32_e32 v107, v107, v91
	v_add_f32_e32 v107, v107, v92
	v_add_f32_e32 v107, v107, v93
	v_add_f32_e32 v107, v107, v94
	v_add_f32_e32 v107, v107, v95
	v_add_f32_e32 v107, v107, v96
	v_add_f32_e32 v107, v107, v97
	v_add_f32_e32 v107, v107, v98
	v_add_f32_e32 v107, v107, v99
	v_add_f32_e32 v107, v107, v100
	v_add_f32_e32 v107, v107, v101
	v_add_f32_e32 v107, v107, v102
	v_add_f32_e32 v107, v107, v103
	v_add_f32_e32 v107, v107, v104
	v_add_f32_e32 v107, v107, v105
	v_cvt_pk_f16_f32 v50, v90, v91
	v_cvt_pk_f16_f32 v51, v92, v93
	v_cvt_pk_f16_f32 v52, v94, v95
	v_cvt_pk_f16_f32 v53, v96, v97
	v_cvt_pk_f16_f32 v54, v98, v99
	v_cvt_pk_f16_f32 v55, v100, v101
	v_cvt_pk_f16_f32 v56, v102, v103
	v_cvt_pk_f16_f32 v57, v104, v105
	ds_read2_b64 v[58:61], v113 offset0:48 offset1:50
	ds_read2_b64 v[62:65], v114 offset0:48 offset1:50
	s_nop 1
	s_waitcnt lgkmcnt(1)
	v_mfma_f32_32x32x16_f16 v[18:33], v[58:61], v[50:53], v[18:33]
	ds_read2_b64 v[58:61], v113 offset0:52 offset1:54
	s_waitcnt lgkmcnt(1)
	v_mfma_f32_32x32x16_f16 v[34:49], v[62:65], v[50:53], v[34:49]
	ds_read2_b64 v[62:65], v114 offset0:52 offset1:54
	s_waitcnt lgkmcnt(1)
	v_mfma_f32_32x32x16_f16 v[18:33], v[58:61], v[54:57], v[18:33]
	s_waitcnt lgkmcnt(0)
	v_mfma_f32_32x32x16_f16 v[34:49], v[62:65], v[54:57], v[34:49]
	ds_read_b128 v[66:69], v112 offset:0
	ds_read_b128 v[70:73], v112 offset:32
	s_waitcnt lgkmcnt(1)
	v_mfma_f32_32x32x16_f16 v[90:105], v[66:69], v[74:77], 0
	ds_read_b128 v[66:69], v112 offset:64
	s_waitcnt lgkmcnt(1)
	v_mfma_f32_32x32x16_f16 v[90:105], v[70:73], v[78:81], v[90:105]
	ds_read_b128 v[70:73], v112 offset:96
	s_waitcnt lgkmcnt(1)
	v_mfma_f32_32x32x16_f16 v[90:105], v[66:69], v[82:85], v[90:105]
	s_waitcnt lgkmcnt(0)
	v_mfma_f32_32x32x16_f16 v[90:105], v[70:73], v[86:89], v[90:105]
	v_fma_f32 v120, v2, s16, -v106
	v_exp_f32_e32 v2, v120
	v_fma_f32 v121, v3, s16, -v106
	v_exp_f32_e32 v3, v121
	v_fma_f32 v122, v4, s16, -v106
	v_exp_f32_e32 v4, v122
	v_fma_f32 v123, v5, s16, -v106
	v_exp_f32_e32 v5, v123
	v_fma_f32 v120, v6, s16, -v106
	v_exp_f32_e32 v6, v120
	v_fma_f32 v121, v7, s16, -v106
	v_exp_f32_e32 v7, v121
	v_fma_f32 v122, v8, s16, -v106
	v_exp_f32_e32 v8, v122
	v_fma_f32 v123, v9, s16, -v106
	v_exp_f32_e32 v9, v123
	v_fma_f32 v120, v10, s16, -v106
	v_exp_f32_e32 v10, v120
	v_fma_f32 v121, v11, s16, -v106
	v_exp_f32_e32 v11, v121
	v_fma_f32 v122, v12, s16, -v106
	v_exp_f32_e32 v12, v122
	v_fma_f32 v123, v13, s16, -v106
	v_exp_f32_e32 v13, v123
	v_fma_f32 v120, v14, s16, -v106
	v_exp_f32_e32 v14, v120
	v_fma_f32 v121, v15, s16, -v106
	v_exp_f32_e32 v15, v121
	v_fma_f32 v122, v16, s16, -v106
	v_exp_f32_e32 v16, v122
	v_fma_f32 v123, v17, s16, -v106
	v_exp_f32_e32 v17, v123
	v_add_f32_e32 v107, v107, v2
	v_add_f32_e32 v107, v107, v3
	v_add_f32_e32 v107, v107, v4
	v_add_f32_e32 v107, v107, v5
	v_add_f32_e32 v107, v107, v6
	v_add_f32_e32 v107, v107, v7
	v_add_f32_e32 v107, v107, v8
	v_add_f32_e32 v107, v107, v9
	v_add_f32_e32 v107, v107, v10
	v_add_f32_e32 v107, v107, v11
	v_add_f32_e32 v107, v107, v12
	v_add_f32_e32 v107, v107, v13
	v_add_f32_e32 v107, v107, v14
	v_add_f32_e32 v107, v107, v15
	v_add_f32_e32 v107, v107, v16
	v_add_f32_e32 v107, v107, v17
	v_cvt_pk_f16_f32 v50, v2, v3
	v_cvt_pk_f16_f32 v51, v4, v5
	v_cvt_pk_f16_f32 v52, v6, v7
	v_cvt_pk_f16_f32 v53, v8, v9
	v_cvt_pk_f16_f32 v54, v10, v11
	v_cvt_pk_f16_f32 v55, v12, v13
	v_cvt_pk_f16_f32 v56, v14, v15
	v_cvt_pk_f16_f32 v57, v16, v17
	ds_read2_b64 v[58:61], v113 offset0:16 offset1:18
	ds_read2_b64 v[62:65], v114 offset0:16 offset1:18
	s_nop 1
	s_waitcnt lgkmcnt(1)
	v_mfma_f32_32x32x16_f16 v[18:33], v[58:61], v[50:53], v[18:33]
	ds_read2_b64 v[58:61], v113 offset0:20 offset1:22
	s_waitcnt lgkmcnt(1)
	v_mfma_f32_32x32x16_f16 v[34:49], v[62:65], v[50:53], v[34:49]
	ds_read2_b64 v[62:65], v114 offset0:20 offset1:22
	s_waitcnt lgkmcnt(1)
	v_mfma_f32_32x32x16_f16 v[18:33], v[58:61], v[54:57], v[18:33]
	s_waitcnt lgkmcnt(0)
	v_mfma_f32_32x32x16_f16 v[34:49], v[62:65], v[54:57], v[34:49]
	ds_read_b128 v[66:69], v112 offset:4608
	ds_read_b128 v[70:73], v112 offset:4640
	s_waitcnt lgkmcnt(1)
	v_mfma_f32_32x32x16_f16 v[2:17], v[66:69], v[74:77], 0
	ds_read_b128 v[66:69], v112 offset:4672
	s_waitcnt lgkmcnt(1)
	v_mfma_f32_32x32x16_f16 v[2:17], v[70:73], v[78:81], v[2:17]
	ds_read_b128 v[70:73], v112 offset:4704
	s_waitcnt lgkmcnt(1)
	v_mfma_f32_32x32x16_f16 v[2:17], v[66:69], v[82:85], v[2:17]
	s_waitcnt lgkmcnt(0)
	v_mfma_f32_32x32x16_f16 v[2:17], v[70:73], v[86:89], v[2:17]
	v_fma_f32 v120, v90, s16, -v106
	v_exp_f32_e32 v90, v120
	v_fma_f32 v121, v91, s16, -v106
	v_exp_f32_e32 v91, v121
	v_fma_f32 v122, v92, s16, -v106
	v_exp_f32_e32 v92, v122
	v_fma_f32 v123, v93, s16, -v106
	v_exp_f32_e32 v93, v123
	v_fma_f32 v120, v94, s16, -v106
	v_exp_f32_e32 v94, v120
	v_fma_f32 v121, v95, s16, -v106
	v_exp_f32_e32 v95, v121
	v_fma_f32 v122, v96, s16, -v106
	v_exp_f32_e32 v96, v122
	v_fma_f32 v123, v97, s16, -v106
	v_exp_f32_e32 v97, v123
	v_fma_f32 v120, v98, s16, -v106
	v_exp_f32_e32 v98, v120
	v_fma_f32 v121, v99, s16, -v106
	v_exp_f32_e32 v99, v121
	v_fma_f32 v122, v100, s16, -v106
	v_exp_f32_e32 v100, v122
	v_fma_f32 v123, v101, s16, -v106
	v_exp_f32_e32 v101, v123
	v_fma_f32 v120, v102, s16, -v106
	v_exp_f32_e32 v102, v120
	v_fma_f32 v121, v103, s16, -v106
	v_exp_f32_e32 v103, v121
	v_fma_f32 v122, v104, s16, -v106
	v_exp_f32_e32 v104, v122
	v_fma_f32 v123, v105, s16, -v106
	v_exp_f32_e32 v105, v123
	v_add_f32_e32 v107, v107, v90
	v_add_f32_e32 v107, v107, v91
	v_add_f32_e32 v107, v107, v92
	v_add_f32_e32 v107, v107, v93
	v_add_f32_e32 v107, v107, v94
	v_add_f32_e32 v107, v107, v95
	v_add_f32_e32 v107, v107, v96
	v_add_f32_e32 v107, v107, v97
	v_add_f32_e32 v107, v107, v98
	v_add_f32_e32 v107, v107, v99
	v_add_f32_e32 v107, v107, v100
	v_add_f32_e32 v107, v107, v101
	v_add_f32_e32 v107, v107, v102
	v_add_f32_e32 v107, v107, v103
	v_add_f32_e32 v107, v107, v104
	v_add_f32_e32 v107, v107, v105
	v_cvt_pk_f16_f32 v50, v90, v91
	v_cvt_pk_f16_f32 v51, v92, v93
	v_cvt_pk_f16_f32 v52, v94, v95
	v_cvt_pk_f16_f32 v53, v96, v97
	v_cvt_pk_f16_f32 v54, v98, v99
	v_cvt_pk_f16_f32 v55, v100, v101
	v_cvt_pk_f16_f32 v56, v102, v103
	v_cvt_pk_f16_f32 v57, v104, v105
	ds_read2_b64 v[58:61], v113 offset0:0 offset1:2
	ds_read2_b64 v[62:65], v114 offset0:0 offset1:2
	s_nop 1
	s_waitcnt lgkmcnt(1)
	v_mfma_f32_32x32x16_f16 v[18:33], v[58:61], v[50:53], v[18:33]
	ds_read2_b64 v[58:61], v113 offset0:4 offset1:6
	s_waitcnt lgkmcnt(1)
	v_mfma_f32_32x32x16_f16 v[34:49], v[62:65], v[50:53], v[34:49]
	ds_read2_b64 v[62:65], v114 offset0:4 offset1:6
	s_waitcnt lgkmcnt(1)
	v_mfma_f32_32x32x16_f16 v[18:33], v[58:61], v[54:57], v[18:33]
	s_waitcnt lgkmcnt(0)
	v_mfma_f32_32x32x16_f16 v[34:49], v[62:65], v[54:57], v[34:49]
	s_nop 15
	s_nop 1
	v_fma_f32 v120, v2, s16, -v106
	v_exp_f32_e32 v2, v120
	v_fma_f32 v121, v3, s16, -v106
	v_exp_f32_e32 v3, v121
	v_fma_f32 v122, v4, s16, -v106
	v_exp_f32_e32 v4, v122
	v_fma_f32 v123, v5, s16, -v106
	v_exp_f32_e32 v5, v123
	v_fma_f32 v120, v6, s16, -v106
	v_exp_f32_e32 v6, v120
	v_fma_f32 v121, v7, s16, -v106
	v_exp_f32_e32 v7, v121
	v_fma_f32 v122, v8, s16, -v106
	v_exp_f32_e32 v8, v122
	v_fma_f32 v123, v9, s16, -v106
	v_exp_f32_e32 v9, v123
	v_fma_f32 v120, v10, s16, -v106
	v_exp_f32_e32 v10, v120
	v_fma_f32 v121, v11, s16, -v106
	v_exp_f32_e32 v11, v121
	v_fma_f32 v122, v12, s16, -v106
	v_exp_f32_e32 v12, v122
	v_fma_f32 v123, v13, s16, -v106
	v_exp_f32_e32 v13, v123
	v_fma_f32 v120, v14, s16, -v106
	v_exp_f32_e32 v14, v120
	v_fma_f32 v121, v15, s16, -v106
	v_exp_f32_e32 v15, v121
	v_fma_f32 v122, v16, s16, -v106
	v_exp_f32_e32 v16, v122
	v_fma_f32 v123, v17, s16, -v106
	v_exp_f32_e32 v17, v123
	v_add_f32_e32 v107, v107, v2
	v_add_f32_e32 v107, v107, v3
	v_add_f32_e32 v107, v107, v4
	v_add_f32_e32 v107, v107, v5
	v_add_f32_e32 v107, v107, v6
	v_add_f32_e32 v107, v107, v7
	v_add_f32_e32 v107, v107, v8
	v_add_f32_e32 v107, v107, v9
	v_add_f32_e32 v107, v107, v10
	v_add_f32_e32 v107, v107, v11
	v_add_f32_e32 v107, v107, v12
	v_add_f32_e32 v107, v107, v13
	v_add_f32_e32 v107, v107, v14
	v_add_f32_e32 v107, v107, v15
	v_add_f32_e32 v107, v107, v16
	v_add_f32_e32 v107, v107, v17
	v_cvt_pk_f16_f32 v50, v2, v3
	v_cvt_pk_f16_f32 v51, v4, v5
	v_cvt_pk_f16_f32 v52, v6, v7
	v_cvt_pk_f16_f32 v53, v8, v9
	v_cvt_pk_f16_f32 v54, v10, v11
	v_cvt_pk_f16_f32 v55, v12, v13
	v_cvt_pk_f16_f32 v56, v14, v15
	v_cvt_pk_f16_f32 v57, v16, v17
	ds_read2_b64 v[58:61], v113 offset0:8 offset1:10
	ds_read2_b64 v[62:65], v114 offset0:8 offset1:10
	s_nop 1
	s_waitcnt lgkmcnt(1)
	v_mfma_f32_32x32x16_f16 v[18:33], v[58:61], v[50:53], v[18:33]
	ds_read2_b64 v[58:61], v113 offset0:12 offset1:14
	s_waitcnt lgkmcnt(1)
	v_mfma_f32_32x32x16_f16 v[34:49], v[62:65], v[50:53], v[34:49]
	ds_read2_b64 v[62:65], v114 offset0:12 offset1:14
	s_waitcnt lgkmcnt(1)
	v_mfma_f32_32x32x16_f16 v[18:33], v[58:61], v[54:57], v[18:33]
	s_waitcnt lgkmcnt(0)
	v_mfma_f32_32x32x16_f16 v[34:49], v[62:65], v[54:57], v[34:49]
	v_mov_b32_e32 v120, v107
	v_mov_b32_e32 v121, v107
	s_nop 1
	v_permlane32_swap_b32_e32 v120, v121
	s_nop 1
	v_add_f32_e32 v107, v120, v121
	v_log_f32_e32 v122, v107
	v_rcp_f32_e32 v123, v107
	s_nop 0
	v_add_f32_e32 v122, v122, v106
	v_fma_f32 v124, -v107, v123, 2.0
	v_mul_f32_e32 v123, v123, v124
	v_lshlrev_b32_e32 v125, 2, v109
	s_mov_b64 s[18:19], exec
	s_and_b64 exec, exec, s[14:15]
	ds_write_b32 v125, v122 offset:61440
	s_mov_b64 exec, s[18:19]
	s_mul_i32 s20, s2, 0x493
	s_lshr_b32 s20, s20, 16
	s_mul_i32 s21, s20, 56
	s_sub_u32 s21, s2, s21
	s_mul_i32 s22, s21, 0x2493
	s_lshr_b32 s22, s22, 16
	s_mul_i32 s23, s22, 7
	s_sub_u32 s23, s21, s23
	s_mul_i32 s24, s23, 0xc5
	s_lshl_b32 s24, s24, 13
	s_lshl_b32 s25, s22, 10
	s_add_u32 s24, s24, s25
	s_lshl_b32 s25, s20, 7
	s_add_u32 s24, s24, s25
	v_lshlrev_b32_e32 v125, 13, v110
	v_add3_u32 v125, v125, s24, v111
	s_nop 15
	s_waitcnt lgkmcnt(0)
	v_mul_f32_e32 v18, v18, v123
	v_mul_f32_e32 v19, v19, v123
	v_mul_f32_e32 v20, v20, v123
	v_mul_f32_e32 v21, v21, v123
	v_mul_f32_e32 v22, v22, v123
	v_mul_f32_e32 v23, v23, v123
	v_mul_f32_e32 v24, v24, v123
	v_mul_f32_e32 v25, v25, v123
	v_cvt_pk_f16_f32 v50, v18, v19
	v_cvt_pk_f16_f32 v51, v20, v21
	v_cvt_pk_f16_f32 v52, v22, v23
	v_cvt_pk_f16_f32 v53, v24, v25
	s_nop 1
	v_permlane32_swap_b32_e32 v50, v52
	v_permlane32_swap_b32_e32 v51, v53
	s_nop 1
	s_and_b64 exec, exec, s[12:13]
	global_store_dwordx4 v125, v[50:53], s[8:9] offset:0
	s_mov_b64 exec, s[18:19]
	s_nop 1
	v_mul_f32_e32 v26, v26, v123
	v_mul_f32_e32 v27, v27, v123
	v_mul_f32_e32 v28, v28, v123
	v_mul_f32_e32 v29, v29, v123
	v_mul_f32_e32 v30, v30, v123
	v_mul_f32_e32 v31, v31, v123
	v_mul_f32_e32 v32, v32, v123
	v_mul_f32_e32 v33, v33, v123
	v_cvt_pk_f16_f32 v54, v26, v27
	v_cvt_pk_f16_f32 v55, v28, v29
	v_cvt_pk_f16_f32 v56, v30, v31
	v_cvt_pk_f16_f32 v57, v32, v33
	s_nop 1
	v_permlane32_swap_b32_e32 v54, v56
	v_permlane32_swap_b32_e32 v55, v57
	s_nop 1
	s_and_b64 exec, exec, s[12:13]
	global_store_dwordx4 v125, v[54:57], s[8:9] offset:32
	s_mov_b64 exec, s[18:19]
	s_nop 1
	v_mul_f32_e32 v34, v34, v123
	v_mul_f32_e32 v35, v35, v123
	v_mul_f32_e32 v36, v36, v123
	v_mul_f32_e32 v37, v37, v123
	v_mul_f32_e32 v38, v38, v123
	v_mul_f32_e32 v39, v39, v123
	v_mul_f32_e32 v40, v40, v123
	v_mul_f32_e32 v41, v41, v123
	v_cvt_pk_f16_f32 v50, v34, v35
	v_cvt_pk_f16_f32 v51, v36, v37
	v_cvt_pk_f16_f32 v52, v38, v39
	v_cvt_pk_f16_f32 v53, v40, v41
	s_nop 1
	v_permlane32_swap_b32_e32 v50, v52
	v_permlane32_swap_b32_e32 v51, v53
	s_nop 1
	s_and_b64 exec, exec, s[12:13]
	global_store_dwordx4 v125, v[50:53], s[8:9] offset:64
	s_mov_b64 exec, s[18:19]
	s_nop 1
	v_mul_f32_e32 v42, v42, v123
	v_mul_f32_e32 v43, v43, v123
	v_mul_f32_e32 v44, v44, v123
	v_mul_f32_e32 v45, v45, v123
	v_mul_f32_e32 v46, v46, v123
	v_mul_f32_e32 v47, v47, v123
	v_mul_f32_e32 v48, v48, v123
	v_mul_f32_e32 v49, v49, v123
	v_cvt_pk_f16_f32 v54, v42, v43
	v_cvt_pk_f16_f32 v55, v44, v45
	v_cvt_pk_f16_f32 v56, v46, v47
	v_cvt_pk_f16_f32 v57, v48, v49
	s_nop 1
	v_permlane32_swap_b32_e32 v54, v56
	v_permlane32_swap_b32_e32 v55, v57
	s_nop 1
	s_and_b64 exec, exec, s[12:13]
	global_store_dwordx4 v125, v[54:57], s[8:9] offset:96
	s_mov_b64 exec, s[18:19]
	s_nop 1
	s_waitcnt lgkmcnt(0)
	s_barrier
	v_lshl_add_u32 v120, v115, 2, v111
	ds_read_b128 v[90:93], v120 offset:61440
	ds_read_b128 v[94:97], v120 offset:61472
	ds_read_b128 v[98:101], v120 offset:61504
	ds_read_b128 v[102:105], v120 offset:61536
	v_lshl_or_b32 v121, v1, 2, v115
	v_mul_u32_u24_e32 v121, 0xc5, v121
	v_add_lshl_u32 v116, v121, v108, 2
	v_add_u32_e32 v117, 0x18a0, v116
	v_add_u32_e32 v118, 0x3140, v116
	v_add_u32_e32 v119, 0x49e0, v116
	s_mul_hi_u32 s21, s2, 0x25e64
	s_mul_i32 s20, s2, 0x25e64
	s_add_u32 s10, s10, s20
	s_addc_u32 s11, s11, s21
	v_cmp_gt_u32_e64 s[22:23], 5, v108
	s_nop 0
	v_readfirstlane_b32 s26, v115
	s_cmp_eq_u32 s26, 0xc0
	s_cbranch_scc1 .Lsp_wave6
	ds_read_b128 v[66:69], v112 offset:0
	ds_read_b128 v[70:73], v112 offset:32
	s_waitcnt lgkmcnt(1)
	v_mfma_f32_32x32x16_f16 v[2:17], v[74:77], v[66:69], 0
	ds_read_b128 v[66:69], v112 offset:64
	s_waitcnt lgkmcnt(1)
	v_mfma_f32_32x32x16_f16 v[2:17], v[78:81], v[70:73], v[2:17]
	ds_read_b128 v[70:73], v112 offset:96
	s_waitcnt lgkmcnt(1)
	v_mfma_f32_32x32x16_f16 v[2:17], v[82:85], v[66:69], v[2:17]
	s_waitcnt lgkmcnt(0)
	v_mfma_f32_32x32x16_f16 v[2:17], v[86:89], v[70:73], v[2:17]
	s_waitcnt lgkmcnt(0)
	ds_read_b128 v[66:69], v112 offset:4608
	ds_read_b128 v[70:73], v112 offset:4640
	s_waitcnt lgkmcnt(1)
	v_mfma_f32_32x32x16_f16 v[18:33], v[74:77], v[66:69], 0
	ds_read_b128 v[66:69], v112 offset:4672
	s_waitcnt lgkmcnt(1)
	v_mfma_f32_32x32x16_f16 v[18:33], v[78:81], v[70:73], v[18:33]
	ds_read_b128 v[70:73], v112 offset:4704
	s_waitcnt lgkmcnt(1)
	v_mfma_f32_32x32x16_f16 v[18:33], v[82:85], v[66:69], v[18:33]
	s_waitcnt lgkmcnt(0)
	v_mfma_f32_32x32x16_f16 v[18:33], v[86:89], v[70:73], v[18:33]
	v_fma_f32 v120, v2, s16, -v90
	v_exp_f32_e32 v2, v120
	v_fma_f32 v121, v3, s16, -v91
	v_exp_f32_e32 v3, v121
	v_fma_f32 v122, v4, s16, -v92
	v_exp_f32_e32 v4, v122
	v_fma_f32 v123, v5, s16, -v93
	v_exp_f32_e32 v5, v123
	v_fma_f32 v120, v6, s16, -v94
	v_exp_f32_e32 v6, v120
	v_fma_f32 v121, v7, s16, -v95
	v_exp_f32_e32 v7, v121
	v_fma_f32 v122, v8, s16, -v96
	v_exp_f32_e32 v8, v122
	v_fma_f32 v123, v9, s16, -v97
	v_exp_f32_e32 v9, v123
	v_fma_f32 v120, v10, s16, -v98
	v_exp_f32_e32 v10, v120
	v_fma_f32 v121, v11, s16, -v99
	v_exp_f32_e32 v11, v121
	v_fma_f32 v122, v12, s16, -v100
	v_exp_f32_e32 v12, v122
	v_fma_f32 v123, v13, s16, -v101
	v_exp_f32_e32 v13, v123
	v_fma_f32 v120, v14, s16, -v102
	v_exp_f32_e32 v14, v120
	v_fma_f32 v121, v15, s16, -v103
	v_exp_f32_e32 v15, v121
	v_fma_f32 v122, v16, s16, -v104
	v_exp_f32_e32 v16, v122
	v_fma_f32 v123, v17, s16, -v105
	v_exp_f32_e32 v17, v123
	global_store_dword v116, v2, s[10:11] offset:0
	global_store_dword v116, v3, s[10:11] offset:788
	global_store_dword v116, v4, s[10:11] offset:1576
	global_store_dword v116, v5, s[10:11] offset:2364
	global_store_dword v117, v6, s[10:11] offset:0
	global_store_dword v117, v7, s[10:11] offset:788
	global_store_dword v117, v8, s[10:11] offset:1576
	global_store_dword v117, v9, s[10:11] offset:2364
	global_store_dword v118, v10, s[10:11] offset:0
	global_store_dword v118, v11, s[10:11] offset:788
	global_store_dword v118, v12, s[10:11] offset:1576
	global_store_dword v118, v13, s[10:11] offset:2364
	global_store_dword v119, v14, s[10:11] offset:0
	global_store_dword v119, v15, s[10:11] offset:788
	global_store_dword v119, v16, s[10:11] offset:1576
	global_store_dword v119, v17, s[10:11] offset:2364
	ds_read_b128 v[66:69], v112 offset:9216
	ds_read_b128 v[70:73], v112 offset:9248
	s_waitcnt lgkmcnt(1)
	v_mfma_f32_32x32x16_f16 v[2:17], v[74:77], v[66:69], 0
	ds_read_b128 v[66:69], v112 offset:9280
	s_waitcnt lgkmcnt(1)
	v_mfma_f32_32x32x16_f16 v[2:17], v[78:81], v[70:73], v[2:17]
	ds_read_b128 v[70:73], v112 offset:9312
	s_waitcnt lgkmcnt(1)
	v_mfma_f32_32x32x16_f16 v[2:17], v[82:85], v[66:69], v[2:17]
	s_waitcnt lgkmcnt(0)
	v_mfma_f32_32x32x16_f16 v[2:17], v[86:89], v[70:73], v[2:17]
	v_fma_f32 v120, v18, s16, -v90
	v_exp_f32_e32 v18, v120
	v_fma_f32 v121, v19, s16, -v91
	v_exp_f32_e32 v19, v121
	v_fma_f32 v122, v20, s16, -v92
	v_exp_f32_e32 v20, v122
	v_fma_f32 v123, v21, s16, -v93
	v_exp_f32_e32 v21, v123
	v_fma_f32 v120, v22, s16, -v94
	v_exp_f32_e32 v22, v120
	v_fma_f32 v121, v23, s16, -v95
	v_exp_f32_e32 v23, v121
	v_fma_f32 v122, v24, s16, -v96
	v_exp_f32_e32 v24, v122
	v_fma_f32 v123, v25, s16, -v97
	v_exp_f32_e32 v25, v123
	v_fma_f32 v120, v26, s16, -v98
	v_exp_f32_e32 v26, v120
	v_fma_f32 v121, v27, s16, -v99
	v_exp_f32_e32 v27, v121
	v_fma_f32 v122, v28, s16, -v100
	v_exp_f32_e32 v28, v122
	v_fma_f32 v123, v29, s16, -v101
	v_exp_f32_e32 v29, v123
	v_fma_f32 v120, v30, s16, -v102
	v_exp_f32_e32 v30, v120
	v_fma_f32 v121, v31, s16, -v103
	v_exp_f32_e32 v31, v121
	v_fma_f32 v122, v32, s16, -v104
	v_exp_f32_e32 v32, v122
	v_fma_f32 v123, v33, s16, -v105
	v_exp_f32_e32 v33, v123
	global_store_dword v116, v18, s[10:11] offset:128
	global_store_dword v116, v19, s[10:11] offset:916
	global_store_dword v116, v20, s[10:11] offset:1704
	global_store_dword v116, v21, s[10:11] offset:2492
	global_store_dword v117, v22, s[10:11] offset:128
	global_store_dword v117, v23, s[10:11] offset:916
	global_store_dword v117, v24, s[10:11] offset:1704
	global_store_dword v117, v25, s[10:11] offset:2492
	global_store_dword v118, v26, s[10:11] offset:128
	global_store_dword v118, v27, s[10:11] offset:916
	global_store_dword v118, v28, s[10:11] offset:1704
	global_store_dword v118, v29, s[10:11] offset:2492
	global_store_dword v119, v30, s[10:11] offset:128
	global_store_dword v119, v31, s[10:11] offset:916
	global_store_dword v119, v32, s[10:11] offset:1704
	global_store_dword v119, v33, s[10:11] offset:2492
	ds_read_b128 v[66:69], v112 offset:13824
	ds_read_b128 v[70:73], v112 offset:13856
	s_waitcnt lgkmcnt(1)
	v_mfma_f32_32x32x16_f16 v[18:33], v[74:77], v[66:69], 0
	ds_read_b128 v[66:69], v112 offset:13888
	s_waitcnt lgkmcnt(1)
	v_mfma_f32_32x32x16_f16 v[18:33], v[78:81], v[70:73], v[18:33]
	ds_read_b128 v[70:73], v112 offset:13920
	s_waitcnt lgkmcnt(1)
	v_mfma_f32_32x32x16_f16 v[18:33], v[82:85], v[66:69], v[18:33]
	s_waitcnt lgkmcnt(0)
	v_mfma_f32_32x32x16_f16 v[18:33], v[86:89], v[70:73], v[18:33]
	v_fma_f32 v120, v2, s16, -v90
	v_exp_f32_e32 v2, v120
	v_fma_f32 v121, v3, s16, -v91
	v_exp_f32_e32 v3, v121
	v_fma_f32 v122, v4, s16, -v92
	v_exp_f32_e32 v4, v122
	v_fma_f32 v123, v5, s16, -v93
	v_exp_f32_e32 v5, v123
	v_fma_f32 v120, v6, s16, -v94
	v_exp_f32_e32 v6, v120
	v_fma_f32 v121, v7, s16, -v95
	v_exp_f32_e32 v7, v121
	v_fma_f32 v122, v8, s16, -v96
	v_exp_f32_e32 v8, v122
	v_fma_f32 v123, v9, s16, -v97
	v_exp_f32_e32 v9, v123
	v_fma_f32 v120, v10, s16, -v98
	v_exp_f32_e32 v10, v120
	v_fma_f32 v121, v11, s16, -v99
	v_exp_f32_e32 v11, v121
	v_fma_f32 v122, v12, s16, -v100
	v_exp_f32_e32 v12, v122
	v_fma_f32 v123, v13, s16, -v101
	v_exp_f32_e32 v13, v123
	v_fma_f32 v120, v14, s16, -v102
	v_exp_f32_e32 v14, v120
	v_fma_f32 v121, v15, s16, -v103
	v_exp_f32_e32 v15, v121
	v_fma_f32 v122, v16, s16, -v104
	v_exp_f32_e32 v16, v122
	v_fma_f32 v123, v17, s16, -v105
	v_exp_f32_e32 v17, v123
	global_store_dword v116, v2, s[10:11] offset:256
	global_store_dword v116, v3, s[10:11] offset:1044
	global_store_dword v116, v4, s[10:11] offset:1832
	global_store_dword v116, v5, s[10:11] offset:2620
	global_store_dword v117, v6, s[10:11] offset:256
	global_store_dword v117, v7, s[10:11] offset:1044
	global_store_dword v117, v8, s[10:11] offset:1832
	global_store_dword v117, v9, s[10:11] offset:2620
	global_store_dword v118, v10, s[10:11] offset:256
	global_store_dword v118, v11, s[10:11] offset:1044
	global_store_dword v118, v12, s[10:11] offset:1832
	global_store_dword v118, v13, s[10:11] offset:2620
	global_store_dword v119, v14, s[10:11] offset:256
	global_store_dword v119, v15, s[10:11] offset:1044
	global_store_dword v119, v16, s[10:11] offset:1832
	global_store_dword v119, v17, s[10:11] offset:2620
	ds_read_b128 v[66:69], v112 offset:18432
	ds_read_b128 v[70:73], v112 offset:18464
	s_waitcnt lgkmcnt(1)
	v_mfma_f32_32x32x16_f16 v[2:17], v[74:77], v[66:69], 0
	ds_read_b128 v[66:69], v112 offset:18496
	s_waitcnt lgkmcnt(1)
	v_mfma_f32_32x32x16_f16 v[2:17], v[78:81], v[70:73], v[2:17]
	ds_read_b128 v[70:73], v112 offset:18528
	s_waitcnt lgkmcnt(1)
	v_mfma_f32_32x32x16_f16 v[2:17], v[82:85], v[66:69], v[2:17]
	s_waitcnt lgkmcnt(0)
	v_mfma_f32_32x32x16_f16 v[2:17], v[86:89], v[70:73], v[2:17]
	v_fma_f32 v120, v18, s16, -v90
	v_exp_f32_e32 v18, v120
	v_fma_f32 v121, v19, s16, -v91
	v_exp_f32_e32 v19, v121
	v_fma_f32 v122, v20, s16, -v92
	v_exp_f32_e32 v20, v122
	v_fma_f32 v123, v21, s16, -v93
	v_exp_f32_e32 v21, v123
	v_fma_f32 v120, v22, s16, -v94
	v_exp_f32_e32 v22, v120
	v_fma_f32 v121, v23, s16, -v95
	v_exp_f32_e32 v23, v121
	v_fma_f32 v122, v24, s16, -v96
	v_exp_f32_e32 v24, v122
	v_fma_f32 v123, v25, s16, -v97
	v_exp_f32_e32 v25, v123
	v_fma_f32 v120, v26, s16, -v98
	v_exp_f32_e32 v26, v120
	v_fma_f32 v121, v27, s16, -v99
	v_exp_f32_e32 v27, v121
	v_fma_f32 v122, v28, s16, -v100
	v_exp_f32_e32 v28, v122
	v_fma_f32 v123, v29, s16, -v101
	v_exp_f32_e32 v29, v123
	v_fma_f32 v120, v30, s16, -v102
	v_exp_f32_e32 v30, v120
	v_fma_f32 v121, v31, s16, -v103
	v_exp_f32_e32 v31, v121
	v_fma_f32 v122, v32, s16, -v104
	v_exp_f32_e32 v32, v122
	v_fma_f32 v123, v33, s16, -v105
	v_exp_f32_e32 v33, v123
	global_store_dword v116, v18, s[10:11] offset:384
	global_store_dword v116, v19, s[10:11] offset:1172
	global_store_dword v116, v20, s[10:11] offset:1960
	global_store_dword v116, v21, s[10:11] offset:2748
	global_store_dword v117, v22, s[10:11] offset:384
	global_store_dword v117, v23, s[10:11] offset:1172
	global_store_dword v117, v24, s[10:11] offset:1960
	global_store_dword v117, v25, s[10:11] offset:2748
	global_store_dword v118, v26, s[10:11] offset:384
	global_store_dword v118, v27, s[10:11] offset:1172
	global_store_dword v118, v28, s[10:11] offset:1960
	global_store_dword v118, v29, s[10:11] offset:2748
	global_store_dword v119, v30, s[10:11] offset:384
	global_store_dword v119, v31, s[10:11] offset:1172
	global_store_dword v119, v32, s[10:11] offset:1960
	global_store_dword v119, v33, s[10:11] offset:2748
	ds_read_b128 v[66:69], v112 offset:23040
	ds_read_b128 v[70:73], v112 offset:23072
	s_waitcnt lgkmcnt(1)
	v_mfma_f32_32x32x16_f16 v[18:33], v[74:77], v[66:69], 0
	ds_read_b128 v[66:69], v112 offset:23104
	s_waitcnt lgkmcnt(1)
	v_mfma_f32_32x32x16_f16 v[18:33], v[78:81], v[70:73], v[18:33]
	ds_read_b128 v[70:73], v112 offset:23136
	s_waitcnt lgkmcnt(1)
	v_mfma_f32_32x32x16_f16 v[18:33], v[82:85], v[66:69], v[18:33]
	s_waitcnt lgkmcnt(0)
	v_mfma_f32_32x32x16_f16 v[18:33], v[86:89], v[70:73], v[18:33]
	v_fma_f32 v120, v2, s16, -v90
	v_exp_f32_e32 v2, v120
	v_fma_f32 v121, v3, s16, -v91
	v_exp_f32_e32 v3, v121
	v_fma_f32 v122, v4, s16, -v92
	v_exp_f32_e32 v4, v122
	v_fma_f32 v123, v5, s16, -v93
	v_exp_f32_e32 v5, v123
	v_fma_f32 v120, v6, s16, -v94
	v_exp_f32_e32 v6, v120
	v_fma_f32 v121, v7, s16, -v95
	v_exp_f32_e32 v7, v121
	v_fma_f32 v122, v8, s16, -v96
	v_exp_f32_e32 v8, v122
	v_fma_f32 v123, v9, s16, -v97
	v_exp_f32_e32 v9, v123
	v_fma_f32 v120, v10, s16, -v98
	v_exp_f32_e32 v10, v120
	v_fma_f32 v121, v11, s16, -v99
	v_exp_f32_e32 v11, v121
	v_fma_f32 v122, v12, s16, -v100
	v_exp_f32_e32 v12, v122
	v_fma_f32 v123, v13, s16, -v101
	v_exp_f32_e32 v13, v123
	v_fma_f32 v120, v14, s16, -v102
	v_exp_f32_e32 v14, v120
	v_fma_f32 v121, v15, s16, -v103
	v_exp_f32_e32 v15, v121
	v_fma_f32 v122, v16, s16, -v104
	v_exp_f32_e32 v16, v122
	v_fma_f32 v123, v17, s16, -v105
	v_exp_f32_e32 v17, v123
	global_store_dword v116, v2, s[10:11] offset:512
	global_store_dword v116, v3, s[10:11] offset:1300
	global_store_dword v116, v4, s[10:11] offset:2088
	global_store_dword v116, v5, s[10:11] offset:2876
	global_store_dword v117, v6, s[10:11] offset:512
	global_store_dword v117, v7, s[10:11] offset:1300
	global_store_dword v117, v8, s[10:11] offset:2088
	global_store_dword v117, v9, s[10:11] offset:2876
	global_store_dword v118, v10, s[10:11] offset:512
	global_store_dword v118, v11, s[10:11] offset:1300
	global_store_dword v118, v12, s[10:11] offset:2088
	global_store_dword v118, v13, s[10:11] offset:2876
	global_store_dword v119, v14, s[10:11] offset:512
	global_store_dword v119, v15, s[10:11] offset:1300
	global_store_dword v119, v16, s[10:11] offset:2088
	global_store_dword v119, v17, s[10:11] offset:2876
	ds_read_b128 v[66:69], v112 offset:27648
	ds_read_b128 v[70:73], v112 offset:27680
	s_waitcnt lgkmcnt(1)
	v_mfma_f32_32x32x16_f16 v[2:17], v[74:77], v[66:69], 0
	ds_read_b128 v[66:69], v112 offset:27712
	s_waitcnt lgkmcnt(1)
	v_mfma_f32_32x32x16_f16 v[2:17], v[78:81], v[70:73], v[2:17]
	ds_read_b128 v[70:73], v112 offset:27744
	s_waitcnt lgkmcnt(1)
	v_mfma_f32_32x32x16_f16 v[2:17], v[82:85], v[66:69], v[2:17]
	s_waitcnt lgkmcnt(0)
	v_mfma_f32_32x32x16_f16 v[2:17], v[86:89], v[70:73], v[2:17]
	v_fma_f32 v120, v18, s16, -v90
	v_exp_f32_e32 v18, v120
	v_fma_f32 v121, v19, s16, -v91
	v_exp_f32_e32 v19, v121
	v_fma_f32 v122, v20, s16, -v92
	v_exp_f32_e32 v20, v122
	v_fma_f32 v123, v21, s16, -v93
	v_exp_f32_e32 v21, v123
	v_fma_f32 v120, v22, s16, -v94
	v_exp_f32_e32 v22, v120
	v_fma_f32 v121, v23, s16, -v95
	v_exp_f32_e32 v23, v121
	v_fma_f32 v122, v24, s16, -v96
	v_exp_f32_e32 v24, v122
	v_fma_f32 v123, v25, s16, -v97
	v_exp_f32_e32 v25, v123
	v_fma_f32 v120, v26, s16, -v98
	v_exp_f32_e32 v26, v120
	v_fma_f32 v121, v27, s16, -v99
	v_exp_f32_e32 v27, v121
	v_fma_f32 v122, v28, s16, -v100
	v_exp_f32_e32 v28, v122
	v_fma_f32 v123, v29, s16, -v101
	v_exp_f32_e32 v29, v123
	v_fma_f32 v120, v30, s16, -v102
	v_exp_f32_e32 v30, v120
	v_fma_f32 v121, v31, s16, -v103
	v_exp_f32_e32 v31, v121
	v_fma_f32 v122, v32, s16, -v104
	v_exp_f32_e32 v32, v122
	v_fma_f32 v123, v33, s16, -v105
	v_exp_f32_e32 v33, v123
	global_store_dword v116, v18, s[10:11] offset:640
	global_store_dword v116, v19, s[10:11] offset:1428
	global_store_dword v116, v20, s[10:11] offset:2216
	global_store_dword v116, v21, s[10:11] offset:3004
	global_store_dword v117, v22, s[10:11] offset:640
	global_store_dword v117, v23, s[10:11] offset:1428
	global_store_dword v117, v24, s[10:11] offset:2216
	global_store_dword v117, v25, s[10:11] offset:3004
	global_store_dword v118, v26, s[10:11] offset:640
	global_store_dword v118, v27, s[10:11] offset:1428
	global_store_dword v118, v28, s[10:11] offset:2216
	global_store_dword v118, v29, s[10:11] offset:3004
	global_store_dword v119, v30, s[10:11] offset:640
	global_store_dword v119, v31, s[10:11] offset:1428
	global_store_dword v119, v32, s[10:11] offset:2216
	global_store_dword v119, v33, s[10:11] offset:3004
	s_nop 15
	s_nop 1
	v_fma_f32 v120, v2, s16, -v90
	v_exp_f32_e32 v2, v120
	v_fma_f32 v121, v3, s16, -v91
	v_exp_f32_e32 v3, v121
	v_fma_f32 v122, v4, s16, -v92
	v_exp_f32_e32 v4, v122
	v_fma_f32 v123, v5, s16, -v93
	v_exp_f32_e32 v5, v123
	v_fma_f32 v120, v6, s16, -v94
	v_exp_f32_e32 v6, v120
	v_fma_f32 v121, v7, s16, -v95
	v_exp_f32_e32 v7, v121
	v_fma_f32 v122, v8, s16, -v96
	v_exp_f32_e32 v8, v122
	v_fma_f32 v123, v9, s16, -v97
	v_exp_f32_e32 v9, v123
	v_fma_f32 v120, v10, s16, -v98
	v_exp_f32_e32 v10, v120
	v_fma_f32 v121, v11, s16, -v99
	v_exp_f32_e32 v11, v121
	v_fma_f32 v122, v12, s16, -v100
	v_exp_f32_e32 v12, v122
	v_fma_f32 v123, v13, s16, -v101
	v_exp_f32_e32 v13, v123
	v_fma_f32 v120, v14, s16, -v102
	v_exp_f32_e32 v14, v120
	v_fma_f32 v121, v15, s16, -v103
	v_exp_f32_e32 v15, v121
	v_fma_f32 v122, v16, s16, -v104
	v_exp_f32_e32 v16, v122
	v_fma_f32 v123, v17, s16, -v105
	v_exp_f32_e32 v17, v123
	s_and_b64 exec, exec, s[22:23]
	global_store_dword v116, v2, s[10:11] offset:768
	global_store_dword v116, v3, s[10:11] offset:1556
	global_store_dword v116, v4, s[10:11] offset:2344
	global_store_dword v116, v5, s[10:11] offset:3132
	global_store_dword v117, v6, s[10:11] offset:768
	global_store_dword v117, v7, s[10:11] offset:1556
	global_store_dword v117, v8, s[10:11] offset:2344
	global_store_dword v117, v9, s[10:11] offset:3132
	global_store_dword v118, v10, s[10:11] offset:768
	global_store_dword v118, v11, s[10:11] offset:1556
	global_store_dword v118, v12, s[10:11] offset:2344
	global_store_dword v118, v13, s[10:11] offset:3132
	global_store_dword v119, v14, s[10:11] offset:768
	global_store_dword v119, v15, s[10:11] offset:1556
	global_store_dword v119, v16, s[10:11] offset:2344
	global_store_dword v119, v17, s[10:11] offset:3132
	s_mov_b64 exec, s[18:19]
	s_endpgm
